# conversion tickets 1-of-2 in layers 1,2 (all conversions handed out alongside the long FoX items; attention-only tail)
# baseline (speedup 1.0000x reference)
.LBB0_789:
	s_or_b64 exec, exec, s[2:3]
	v_readlane_b32 s2, v253, 55
	s_waitcnt lgkmcnt(0)
	s_barrier
	v_mov_b32_e32 v0, s2
	v_readlane_b32 s2, v253, 54
	ds_read_b32 v0, v0
	s_nop 0
	v_mov_b32_e32 v1, s2
	ds_read_b32 v1, v1
	s_waitcnt lgkmcnt(0)
	s_barrier
	v_add_u32_e32 v201, 0x580, v0
	s_nop 0
	v_readfirstlane_b32 s100, v201
	v_readlane_b32 s101, v254, 38
	s_nop 3
	s_movk_i32 vcc_lo, 0x4c0
	s_movk_i32 vcc_hi, 0x980
	s_cmp_eq_u32 s101, 0
	s_cselect_b32 vcc_lo, 0xac0, vcc_lo
	s_cselect_b32 vcc_hi, 0x1580, vcc_hi
	s_cmp_eq_u32 s101, 3
	s_cselect_b32 vcc_lo, 0, vcc_lo
	s_cselect_b32 vcc_hi, 0, vcc_hi
	s_add_i32 vcc_lo, s100, vcc_lo
	s_max_u32 vcc_lo, vcc_lo, vcc_hi
	v_mov_b32_e32 v201, vcc_lo
	v_readfirstlane_b32 s30, v0
	v_cmp_ge_i32_e32 vcc, v1, v201
	v_readfirstlane_b32 s24, v1
	s_cbranch_vccnz .LBB0_931
	s_add_u32 s31, s4, 0x37b00000
	s_addc_u32 s34, s5, 0
	s_add_i32 s35, s30, 0x480
	s_add_u32 s44, s4, 0x61800000
	s_addc_u32 s45, s5, 0
	s_add_u32 s46, s4, 0x42c00000
	s_addc_u32 s47, s5, 0
	s_add_u32 s10, s4, 0x66d00000
	s_addc_u32 s11, s5, 0
	s_add_u32 s48, s4, 0x61640000
	s_movk_i32 s2, 0x100
	s_addc_u32 s49, s5, 0
	v_cmp_gt_i32_e64 s[38:39], s2, v199
	s_add_i32 s2, 0, 0x14800
	v_add_u32_e32 v214, s2, v200
	s_add_i32 s2, 0, 0x16800
	s_cmp_lg_u32 0, -1
	v_lshlrev_b32_e32 v3, 1, v199
	v_lshlrev_b32_e32 v211, 4, v199
	s_cselect_b32 s3, 0, 0
	v_lshlrev_b32_e32 v0, 3, v199
	v_lshlrev_b32_e32 v1, 10, v101
	v_lshlrev_b32_e32 v2, 4, v198
	v_and_b32_e32 v3, 32, v3
	v_and_b32_e32 v5, 0xc0, v211
	s_addk_i32 s3, 0x6000
	v_and_b32_e32 v210, 24, v0
	v_lshl_or_b32 v5, v101, 8, v5
	v_add3_u32 v213, 0, v1, v2
	v_add_u32_e32 v1, s3, v3
	v_add3_u32 v217, v1, v210, v5
	v_lshrrev_b32_e32 v1, 3, v100
	v_lshl_add_u32 v215, v198, 2, s2
	v_and_b32_e32 v218, 56, v0
	v_lshl_add_u32 v220, v1, 2, s2
	s_add_i32 s2, 0, 0x14a00
	v_add_u32_e32 v4, 0, v3
	v_lshlrev_b32_e32 v96, 1, v218
	v_add_u32_e32 v221, s2, v200
	s_add_i32 s2, 0, 0x14900
	v_ashrrev_i32_e32 v203, 31, v202
	v_lshlrev_b32_e32 v208, 9, v100
	v_lshrrev_b32_e32 v209, 2, v100
	v_add3_u32 v212, v4, v210, v5
	v_cmp_gt_u32_e64 s[40:41], 32, v100
	v_cmp_lt_u32_e64 s[42:43], 31, v100
	v_or_b32_e32 v216, 0xc0, v206
	v_lshl_add_u64 v[204:205], s[4:5], 0, v[96:97]
	v_lshlrev_b32_e32 v219, 7, v1
	v_add_u32_e32 v222, s2, v200
	v_lshlrev_b32_e32 v96, 1, v98
	s_branch .LBB0_792

.LBB0_796:
	s_or_b64 exec, exec, s[2:3]
	v_readlane_b32 s101, v254, 38
	s_nop 3
	s_cmp_eq_u32 s101, 3
	s_cbranch_scc1 .Lc3_attn
	s_cmp_eq_u32 s101, 0
	s_cbranch_scc1 .Lc3_l0
	s_cmpk_lt_u32 s24, 0x980
	s_cbranch_scc0 .Lc3_late
	s_lshr_b32 s101, s24, 1
	s_bitcmp1_b32 s24, 0
	s_cbranch_scc1 .Lc3_entry
	s_sub_i32 s24, s24, s101
	s_branch .Lc3_chk
